# dilated attention passes: the unconditional K-tile reload on each pattern's last tile (16 loads + 80 address VALU, never consumed) is branched over
# speedup vs baseline: 1.0029x; 1.0029x over previous
; #define FA_SBAR() __builtin_amdgcn_sched_barrier(0)
; #define AA_LOADKC(tile_) do { _Pragma("unroll") for (int i_ = 0; i_ < 16; ++i_) { int tk = cls + ((base + (tile_) * 64 + 4 * i_ + vkey) << sh); tk = tk < 0 ? 0 : (tk > SEQ - 1 ? SEQ - 1 : tk); \
;                     kc[i_] = *(const v4u*)(Zbc + (unsigned)tk * (NA * 2) + (ZA_K + vch * 8) * 2); } } while (0)
; #define AA_WRITEV(vv_, i0_) do { _Pragma("unroll") for (int i_ = 0; i_ < 8; ++i_) { const int i = (i0_) + i_; *(LAS v4u*)(Vl + vstb + ((i & 1) + 2 * (i >> 2)) * 2048 + ((i >> 1) & 1) * 256) = vv_[i_]; } } while (0)
; __device__ __forceinline__ void partialSM(f32x16& p0, f32x16& p1, float& m_reg, float& mn, float& alpha, const float C, const float thr) {
;     ...
;   for (int r = 0; r < 16; ++r) p0[r] = fmaf(p0[r], C, mnC);
; #pragma unroll
;   for (int r = 0; r < 16; ++r) p1[r] = fmaf(p1[r], C, mnC);
; #pragma unroll
;   for (int r = 0; r < 16; ++r) p0[r] = __builtin_amdgcn_exp2f(p0[r]);
; }
; __device__ __forceinline__ void finishSM(f32x16& p0, f32x16& p1, float alpha, float& l_reg, bf16x8& pa0, bf16x8& pa1, bf16x8& pa2, bf16x8& pa3) {
; #pragma unroll
;   for (int r = 0; r < 16; ++r) p1[r] = __builtin_amdgcn_exp2f(p1[r]);
;   float ps = 0;
; #pragma unroll
;   for (int r = 0; r < 16; ++r) ps += p0[r];
; #pragma unroll
;   for (int r = 0; r < 16; ++r) ps += p1[r];
;   { auto rr = __builtin_amdgcn_permlane32_swap(__float_as_uint(ps), __float_as_uint(ps), false, false);
;     ps = __uint_as_float(rr[0]) + __uint_as_float(rr[1]); }
;   l_reg = l_reg * alpha + ps;
;   FA_PK4(p0, 0, pa0); FA_PK4(p0, 8, pa1); FA_PK4(p1, 0, pa2); FA_PK4(p1, 8, pa3);
; template <int PASS>
; __device__ __forceinline__ void attn_a_pass(LAS unsigned char* lds_all, const bf16* ZA, bf16* Oabc, float* ML, const float* rel_bias, int gw, int ngw, int xcd, int inx, int tid) {
;     ...
;                 AA_WRITEV(vbq, 8);
;                 asm volatile("s_waitcnt lgkmcnt(0)" ::: "memory"); FA_SBAR();
;                 { const int tn = (tile + 1 < ntile) ? tile + 1 : tile; AA_LOADKC(tn); }
.LBB0_943:
	v_cndmask_b32_e64 v194, v0, v194, s[6:7]
	v_mul_f32_e32 v0, 0xbe0293ee, v194
	v_fmamk_f32 v80, v162, 0x3e0293ee, v0
	v_fmamk_f32 v81, v163, 0x3e0293ee, v0
	v_fmamk_f32 v84, v84, 0x3e0293ee, v0
	v_fmamk_f32 v85, v85, 0x3e0293ee, v0
	v_fmamk_f32 v86, v86, 0x3e0293ee, v0
	v_fmamk_f32 v87, v87, 0x3e0293ee, v0
	v_fmamk_f32 v88, v88, 0x3e0293ee, v0
	v_fmamk_f32 v89, v89, 0x3e0293ee, v0
	v_fmamk_f32 v90, v90, 0x3e0293ee, v0
	v_fmamk_f32 v91, v91, 0x3e0293ee, v0
	v_fmamk_f32 v92, v92, 0x3e0293ee, v0
	v_fmamk_f32 v93, v93, 0x3e0293ee, v0
	v_fmamk_f32 v94, v94, 0x3e0293ee, v0
	v_fmamk_f32 v95, v95, 0x3e0293ee, v0
	v_fmamk_f32 v82, v82, 0x3e0293ee, v0
	v_fmamk_f32 v83, v83, 0x3e0293ee, v0
	v_fmamk_f32 v96, v96, 0x3e0293ee, v0
	v_fmamk_f32 v97, v97, 0x3e0293ee, v0
	v_fmamk_f32 v68, v68, 0x3e0293ee, v0
	v_fmamk_f32 v69, v69, 0x3e0293ee, v0
	v_fmamk_f32 v70, v70, 0x3e0293ee, v0
	v_fmamk_f32 v71, v71, 0x3e0293ee, v0
	v_fmamk_f32 v72, v72, 0x3e0293ee, v0
	v_fmamk_f32 v73, v73, 0x3e0293ee, v0
	v_fmamk_f32 v74, v74, 0x3e0293ee, v0
	v_fmamk_f32 v75, v75, 0x3e0293ee, v0
	v_fmamk_f32 v76, v76, 0x3e0293ee, v0
	v_fmamk_f32 v77, v77, 0x3e0293ee, v0
	v_fmamk_f32 v78, v78, 0x3e0293ee, v0
	v_fmamk_f32 v79, v79, 0x3e0293ee, v0
	v_fmamk_f32 v66, v66, 0x3e0293ee, v0
	v_fmac_f32_e32 v0, 0x3e0293ee, v67
	v_exp_f32_e32 v67, v80
	v_exp_f32_e32 v80, v81
	v_exp_f32_e32 v81, v84
	v_exp_f32_e32 v84, v85
	v_exp_f32_e32 v85, v86
	v_exp_f32_e32 v173, v66
	v_add_f32_e32 v66, 0, v67
	v_exp_f32_e32 v86, v87
	v_add_f32_e32 v66, v80, v66
	v_exp_f32_e32 v87, v88
	v_add_f32_e32 v66, v81, v66
	v_exp_f32_e32 v88, v89
	v_add_f32_e32 v66, v84, v66
	v_exp_f32_e32 v89, v90
	v_add_f32_e32 v66, v85, v66
	v_exp_f32_e32 v90, v91
	v_add_f32_e32 v66, v86, v66
	v_exp_f32_e32 v91, v92
	v_add_f32_e32 v66, v87, v66
	v_exp_f32_e32 v92, v93
	v_add_f32_e32 v66, v88, v66
	v_exp_f32_e32 v93, v94
	v_add_f32_e32 v66, v89, v66
	v_exp_f32_e32 v94, v95
	v_add_f32_e32 v66, v90, v66
	v_exp_f32_e32 v82, v82
	v_add_f32_e32 v66, v91, v66
	v_exp_f32_e32 v83, v83
	v_add_f32_e32 v66, v92, v66
	v_exp_f32_e32 v95, v96
	v_add_f32_e32 v66, v93, v66
	v_exp_f32_e32 v96, v97
	v_add_f32_e32 v66, v94, v66
	v_exp_f32_e32 v97, v68
	v_add_f32_e32 v66, v82, v66
	v_exp_f32_e32 v162, v69
	v_add_f32_e32 v66, v83, v66
	v_exp_f32_e32 v163, v70
	v_add_f32_e32 v66, v95, v66
	v_exp_f32_e32 v164, v71
	v_add_f32_e32 v66, v96, v66
	v_exp_f32_e32 v165, v72
	v_add_f32_e32 v66, v97, v66
	v_exp_f32_e32 v166, v73
	v_add_f32_e32 v66, v162, v66
	v_exp_f32_e32 v167, v74
	v_add_f32_e32 v66, v163, v66
	v_exp_f32_e32 v168, v75
	v_add_f32_e32 v66, v164, v66
	v_exp_f32_e32 v169, v76
	v_add_f32_e32 v66, v165, v66
	v_exp_f32_e32 v170, v77
	v_add_f32_e32 v66, v166, v66
	v_exp_f32_e32 v171, v78
	v_add_f32_e32 v66, v167, v66
	v_exp_f32_e32 v172, v79
	v_add_f32_e32 v66, v168, v66
	v_add_f32_e32 v66, v169, v66
	v_exp_f32_e32 v0, v0
	v_add_f32_e32 v66, v170, v66
	v_add_f32_e32 v66, v171, v66
	v_add_f32_e32 v66, v172, v66
	v_add_f32_e32 v66, v173, v66
	v_add_f32_e32 v195, v0, v66
	v_mov_b32_e32 v213, v195
	s_nop 1
	v_permlane32_swap_b32_e32 v195, v213
	v_cvt_pk_bf16_f32 v66, v67, v80
	v_cvt_pk_bf16_f32 v67, v81, v84
	v_cvt_pk_bf16_f32 v68, v85, v86
	v_cvt_pk_bf16_f32 v69, v87, v88
	v_cvt_pk_bf16_f32 v70, v89, v90
	v_cvt_pk_bf16_f32 v71, v91, v92
	v_cvt_pk_bf16_f32 v72, v93, v94
	v_cvt_pk_bf16_f32 v73, v82, v83
	v_cvt_pk_bf16_f32 v74, v95, v96
	v_cvt_pk_bf16_f32 v75, v97, v162
	v_cvt_pk_bf16_f32 v76, v163, v164
	v_cvt_pk_bf16_f32 v77, v165, v166
	v_cvt_pk_bf16_f32 v78, v167, v168
	v_cvt_pk_bf16_f32 v79, v169, v170
	v_cvt_pk_bf16_f32 v80, v171, v172
	v_cvt_pk_bf16_f32 v81, v173, v0
	s_nop 0
	v_permlane32_swap_b32_e32 v66, v68
	v_permlane32_swap_b32_e32 v67, v69
	v_permlane32_swap_b32_e32 v70, v72
	v_permlane32_swap_b32_e32 v71, v73
	v_permlane32_swap_b32_e32 v74, v76
	v_permlane32_swap_b32_e32 v75, v77
	v_permlane32_swap_b32_e32 v78, v80
	v_permlane32_swap_b32_e32 v79, v81
	s_waitcnt vmcnt(7)
	ds_write_b128 v210, v[130:133] offset:8192
	s_waitcnt vmcnt(6)
	ds_write_b128 v210, v[134:137] offset:10240
	s_waitcnt vmcnt(5)
	ds_write_b128 v210, v[138:141] offset:8448
	s_waitcnt vmcnt(4)
	ds_write_b128 v210, v[142:145] offset:10496
	s_waitcnt vmcnt(3)
	ds_write_b128 v210, v[146:149] offset:12288
	s_waitcnt vmcnt(2)
	ds_write_b128 v210, v[150:153] offset:14336
	s_waitcnt vmcnt(1)
	ds_write_b128 v210, v[154:157] offset:12544
	s_waitcnt vmcnt(0)
	ds_write_b128 v210, v[158:161] offset:14592
	s_waitcnt lgkmcnt(0)
	s_cmpk_eq_i32 s69, 0xfe00
	s_cselect_b64 s[6:7], -1, 0
	s_and_b64 vcc, s[6:7], exec
	s_cselect_b32 s6, 0x80, s82
	s_cbranch_vccnz .Ldil1_noreload
; #define AA_LOADKC(tile_) do { _Pragma("unroll") for (int i_ = 0; i_ < 16; ++i_) { int tk = cls + ((base + (tile_) * 64 + 4 * i_ + vkey) << sh); tk = tk < 0 ? 0 : (tk > SEQ - 1 ? SEQ - 1 : tk); \
;                     kc[i_] = *(const v4u*)(Zbc + (unsigned)tk * (NA * 2) + (ZA_K + vch * 8) * 2); } } while (0)
; template <int PASS>
; __device__ __forceinline__ void attn_a_pass(LAS unsigned char* lds_all, const bf16* ZA, bf16* Oabc, float* ML, const float* rel_bias, int gw, int ngw, int xcd, int inx, int tid) {
;     ...
;                 { const int tn = (tile + 1 < ntile) ? tile + 1 : tile; AA_LOADKC(tn); }
	v_add_u32_e32 v172, s6, v197
	v_med3_i32 v0, v172, 0, v230
	v_mul_u32_u24_e32 v0, 0x1800, v0
	v_lshl_add_u64 v[82:83], v[192:193], 0, v[0:1]
	v_max_i32_e32 v0, -4, v172
	v_add_u32_e32 v0, 4, v0
	v_min_u32_e32 v0, 0xfff, v0
	v_mul_u32_u24_e32 v0, 0x1800, v0
	v_lshl_add_u64 v[86:87], v[192:193], 0, v[0:1]
	v_max_i32_e32 v0, -8, v172
	v_add_u32_e32 v0, 8, v0
	v_min_u32_e32 v0, 0xfff, v0
	v_mul_u32_u24_e32 v0, 0x1800, v0
	v_lshl_add_u64 v[90:91], v[192:193], 0, v[0:1]
	v_max_i32_e32 v0, -12, v172
	v_add_u32_e32 v0, 12, v0
	v_min_u32_e32 v0, 0xfff, v0
	v_mul_u32_u24_e32 v0, 0x1800, v0
	v_lshl_add_u64 v[94:95], v[192:193], 0, v[0:1]
	v_max_i32_e32 v0, -16, v172
	v_add_u32_e32 v0, 16, v0
	v_min_u32_e32 v0, 0xfff, v0
	v_mul_u32_u24_e32 v0, 0x1800, v0
	v_lshl_add_u64 v[130:131], v[192:193], 0, v[0:1]
	v_max_i32_e32 v0, 0xffffffec, v172
	v_add_u32_e32 v0, 20, v0
	v_min_u32_e32 v0, 0xfff, v0
	v_mul_u32_u24_e32 v0, 0x1800, v0
	v_lshl_add_u64 v[134:135], v[192:193], 0, v[0:1]
	v_max_i32_e32 v0, 0xffffffe8, v172
	v_add_u32_e32 v0, 24, v0
	v_min_u32_e32 v0, 0xfff, v0
	v_mul_u32_u24_e32 v0, 0x1800, v0
	v_lshl_add_u64 v[138:139], v[192:193], 0, v[0:1]
	v_max_i32_e32 v0, 0xffffffe4, v172
	v_add_u32_e32 v0, 28, v0
	v_min_u32_e32 v0, 0xfff, v0
	v_mul_u32_u24_e32 v0, 0x1800, v0
	v_lshl_add_u64 v[142:143], v[192:193], 0, v[0:1]
	v_max_i32_e32 v0, 0xffffffe0, v172
	v_add_u32_e32 v0, 32, v0
	v_min_u32_e32 v0, 0xfff, v0
	v_mul_u32_u24_e32 v0, 0x1800, v0
	v_lshl_add_u64 v[146:147], v[192:193], 0, v[0:1]
	v_max_i32_e32 v0, 0xffffffdc, v172
	v_add_u32_e32 v0, 36, v0
	v_min_u32_e32 v0, 0xfff, v0
	v_mul_u32_u24_e32 v0, 0x1800, v0
	v_lshl_add_u64 v[150:151], v[192:193], 0, v[0:1]
	v_max_i32_e32 v0, 0xffffffd8, v172
	v_add_u32_e32 v0, 40, v0
	v_min_u32_e32 v0, 0xfff, v0
	v_mul_u32_u24_e32 v0, 0x1800, v0
	v_lshl_add_u64 v[154:155], v[192:193], 0, v[0:1]
	v_max_i32_e32 v0, 0xffffffd4, v172
	v_add_u32_e32 v0, 44, v0
	v_min_u32_e32 v0, 0xfff, v0
	v_mul_u32_u24_e32 v0, 0x1800, v0
	v_lshl_add_u64 v[158:159], v[192:193], 0, v[0:1]
	v_max_i32_e32 v0, 0xffffffd0, v172
	v_add_u32_e32 v0, 48, v0
	v_min_u32_e32 v0, 0xfff, v0
	v_mul_u32_u24_e32 v0, 0x1800, v0
	v_lshl_add_u64 v[162:163], v[192:193], 0, v[0:1]
	v_max_i32_e32 v0, 0xffffffcc, v172
	v_add_u32_e32 v0, 52, v0
	v_min_u32_e32 v0, 0xfff, v0
	v_mul_u32_u24_e32 v0, 0x1800, v0
	v_lshl_add_u64 v[166:167], v[192:193], 0, v[0:1]
	v_max_i32_e32 v0, 0xffffffc8, v172
	v_add_u32_e32 v0, 56, v0
	v_min_u32_e32 v0, 0xfff, v0
	v_mul_u32_u24_e32 v0, 0x1800, v0
	v_lshl_add_u64 v[170:171], v[192:193], 0, v[0:1]
	v_max_i32_e32 v0, 0xffffffc4, v172
	v_add_u32_e32 v0, 60, v0
	v_min_u32_e32 v0, 0xfff, v0
	v_mul_u32_u24_e32 v0, 0x1800, v0
	v_lshl_add_u64 v[174:175], v[192:193], 0, v[0:1]
	global_load_dwordx4 v[82:85], v[82:83], off offset:2048
	s_nop 0
	global_load_dwordx4 v[86:89], v[86:87], off offset:2048
	s_nop 0
	global_load_dwordx4 v[90:93], v[90:91], off offset:2048
	s_nop 0
	global_load_dwordx4 v[94:97], v[94:95], off offset:2048
	s_nop 0
	global_load_dwordx4 v[130:133], v[130:131], off offset:2048
	s_nop 0
	global_load_dwordx4 v[134:137], v[134:135], off offset:2048
	s_nop 0
	global_load_dwordx4 v[138:141], v[138:139], off offset:2048
	s_nop 0
	global_load_dwordx4 v[142:145], v[142:143], off offset:2048
	s_nop 0
	global_load_dwordx4 v[146:149], v[146:147], off offset:2048
	s_nop 0
	global_load_dwordx4 v[150:153], v[150:151], off offset:2048
	s_nop 0
	global_load_dwordx4 v[154:157], v[154:155], off offset:2048
	s_nop 0
	global_load_dwordx4 v[158:161], v[158:159], off offset:2048
	s_nop 0
	global_load_dwordx4 v[162:165], v[162:163], off offset:2048
	s_nop 0
	global_load_dwordx4 v[166:169], v[166:167], off offset:2048
	s_nop 0
	global_load_dwordx4 v[170:173], v[170:171], off offset:2048
	s_nop 0
	global_load_dwordx4 v[174:177], v[174:175], off offset:2048
; #define FA_SBAR() __builtin_amdgcn_sched_barrier(0)
; #define AA_WRITEKC() do { _Pragma("unroll") for (int i_ = 0; i_ < 16; ++i_) *(LAS v4u*)(Vl + i_ * 1024 + ((i_ & 1) ? (kst0 ^ 64) : kst0)) = kc[i_]; } while (0)
;   s16x4 l0 = tr_read<BASE + v_rd_off(D0, 0, 0)>(vb), h0 = tr_read<BASE + v_rd_off(D0, 0, 1)>(vb), l1 = tr_read<BASE + v_rd_off(D0, 1, 0)>(vb), h1 = tr_read<BASE + v_rd_off(D0, 1, 1)>(vb);
;   s16x4 l2 = tr_read<BASE + v_rd_off(D0, 2, 0)>(vb), h2 = tr_read<BASE + v_rd_off(D0, 2, 1)>(vb), l3 = tr_read<BASE + v_rd_off(D0, 3, 0)>(vb), h3 = tr_read<BASE + v_rd_off(D0, 3, 1)>(vb);
;   asm volatile("s_waitcnt lgkmcnt(0)" : "+v"(l0), "+v"(h0), "+v"(l1), "+v"(h1), "+v"(l2), "+v"(h2), "+v"(l3), "+v"(h3) :: "memory"); FA_SBAR();
;     ...
;   od = __builtin_amdgcn_mfma_f32_32x32x16_bf16(pa0, FA_PK(l0, h0), od, 0, 0, 0);
;   od = __builtin_amdgcn_mfma_f32_32x32x16_bf16(pa1, FA_PK(l1, h1), od, 0, 0, 0);
;   od = __builtin_amdgcn_mfma_f32_32x32x16_bf16(pa2, FA_PK(l2, h2), od, 0, 0, 0);
;   od = __builtin_amdgcn_mfma_f32_32x32x16_bf16(pa3, FA_PK(l3, h3), od, 0, 0, 0);
;     ...
; }
;   pv_one<0, BASE>(o[0], vb, pa0, pa1, pa2, pa3); pv_one<1, BASE>(o[1], vb, pa0, pa1, pa2, pa3); pv_one<2, BASE>(o[2], vb, pa0, pa1, pa2, pa3); pv_one<3, BASE>(o[3], vb, pa0, pa1, pa2, pa3);
; template <int PASS>
; __device__ __forceinline__ void attn_a_pass(LAS unsigned char* lds_all, const bf16* ZA, bf16* Oabc, float* ML, const float* rel_bias, int gw, int ngw, int xcd, int inx, int tid) {
;     ...
;                 pv_d0(o, vb, pa0, pa1, pa2, pa3);
;                 FA_SBAR();
;                 if (tile + 1 < ntile) AA_WRITEKC();
.Ldil1_noreload:
	ds_read_b64_tr_b16 v[214:215], v199 offset:0
	ds_read_b64_tr_b16 v[216:217], v199 offset:0x800
	ds_read_b64_tr_b16 v[236:237], v199 offset:0x1000
	ds_read_b64_tr_b16 v[238:239], v199 offset:0x1800
	ds_read_b64_tr_b16 v[240:241], v199 offset:0x2000
	ds_read_b64_tr_b16 v[242:243], v199 offset:0x2800
	ds_read_b64_tr_b16 v[244:245], v199 offset:0x3000
	ds_read_b64_tr_b16 v[246:247], v199 offset:0x3800
	s_nop 0
	s_waitcnt lgkmcnt(6)
	s_nop 0
	v_mfma_f32_32x32x16_bf16 v[50:65], v[66:69], v[214:217], v[50:65]
	ds_read_b64_tr_b16 v[214:215], v199 offset:0x200
	ds_read_b64_tr_b16 v[216:217], v199 offset:0xa00
	s_waitcnt lgkmcnt(6)
	v_mfma_f32_32x32x16_bf16 v[50:65], v[70:73], v[236:239], v[50:65]
	ds_read_b64_tr_b16 v[236:237], v199 offset:0x1200
	ds_read_b64_tr_b16 v[238:239], v199 offset:0x1a00
	s_waitcnt lgkmcnt(6)
	v_mfma_f32_32x32x16_bf16 v[50:65], v[74:77], v[240:243], v[50:65]
	ds_read_b64_tr_b16 v[240:241], v199 offset:0x2200
	ds_read_b64_tr_b16 v[242:243], v199 offset:0x2a00
	s_waitcnt lgkmcnt(6)
	v_mfma_f32_32x32x16_bf16 v[50:65], v[78:81], v[244:247], v[50:65]
	ds_read_b64_tr_b16 v[244:245], v199 offset:0x3200
	ds_read_b64_tr_b16 v[246:247], v199 offset:0x3a00
	s_nop 0
	s_waitcnt lgkmcnt(6)
	s_nop 0
	v_mfma_f32_32x32x16_bf16 v[34:49], v[66:69], v[214:217], v[34:49]
	ds_read_b64_tr_b16 v[214:215], v199 offset:0x400
	ds_read_b64_tr_b16 v[216:217], v199 offset:0xc00
	s_waitcnt lgkmcnt(6)
	v_mfma_f32_32x32x16_bf16 v[34:49], v[70:73], v[236:239], v[34:49]
	ds_read_b64_tr_b16 v[236:237], v199 offset:0x1400
	ds_read_b64_tr_b16 v[238:239], v199 offset:0x1c00
	s_waitcnt lgkmcnt(6)
	v_mfma_f32_32x32x16_bf16 v[34:49], v[74:77], v[240:243], v[34:49]
	ds_read_b64_tr_b16 v[240:241], v199 offset:0x2400
	ds_read_b64_tr_b16 v[242:243], v199 offset:0x2c00
	s_waitcnt lgkmcnt(6)
	v_mfma_f32_32x32x16_bf16 v[34:49], v[78:81], v[244:247], v[34:49]
	ds_read_b64_tr_b16 v[244:245], v199 offset:0x3400
	ds_read_b64_tr_b16 v[246:247], v199 offset:0x3c00
	s_nop 0
	s_waitcnt lgkmcnt(6)
	s_nop 0
	v_mfma_f32_32x32x16_bf16 v[18:33], v[66:69], v[214:217], v[18:33]
	ds_read_b64_tr_b16 v[214:215], v199 offset:0x600
	ds_read_b64_tr_b16 v[216:217], v199 offset:0xe00
	s_waitcnt lgkmcnt(6)
	v_mfma_f32_32x32x16_bf16 v[18:33], v[70:73], v[236:239], v[18:33]
	ds_read_b64_tr_b16 v[236:237], v199 offset:0x1600
	ds_read_b64_tr_b16 v[238:239], v199 offset:0x1e00
	s_waitcnt lgkmcnt(6)
	v_mfma_f32_32x32x16_bf16 v[18:33], v[74:77], v[240:243], v[18:33]
	ds_read_b64_tr_b16 v[240:241], v199 offset:0x2600
	ds_read_b64_tr_b16 v[242:243], v199 offset:0x2e00
	s_waitcnt lgkmcnt(6)
	v_mfma_f32_32x32x16_bf16 v[18:33], v[78:81], v[244:247], v[18:33]
	ds_read_b64_tr_b16 v[244:245], v199 offset:0x3600
	ds_read_b64_tr_b16 v[246:247], v199 offset:0x3e00
	s_nop 0
	s_waitcnt lgkmcnt(6)
	s_nop 0
	v_mfma_f32_32x32x16_bf16 v[2:17], v[66:69], v[214:217], v[2:17]
	s_waitcnt lgkmcnt(4)
	v_mfma_f32_32x32x16_bf16 v[2:17], v[70:73], v[236:239], v[2:17]
	s_waitcnt lgkmcnt(2)
	v_mfma_f32_32x32x16_bf16 v[2:17], v[74:77], v[240:243], v[2:17]
	s_waitcnt lgkmcnt(0)
	v_mfma_f32_32x32x16_bf16 v[2:17], v[78:81], v[244:247], v[2:17]
	s_cbranch_vccnz .LBB0_945
	s_waitcnt vmcnt(15)
	ds_write_b128 v200, v[82:85]
	s_waitcnt vmcnt(14)
	ds_write_b128 v201, v[86:89] offset:1024
	s_waitcnt vmcnt(13)
	ds_write_b128 v200, v[90:93] offset:2048
	s_waitcnt vmcnt(12)
	ds_write_b128 v201, v[94:97] offset:3072
	s_waitcnt vmcnt(11)
	ds_write_b128 v200, v[130:133] offset:4096
	s_waitcnt vmcnt(10)
	ds_write_b128 v201, v[134:137] offset:5120
	s_waitcnt vmcnt(9)
	ds_write_b128 v200, v[138:141] offset:6144
	s_waitcnt vmcnt(8)
	ds_write_b128 v201, v[142:145] offset:7168
	s_waitcnt vmcnt(7)
	ds_write_b128 v200, v[146:149] offset:8192
	s_waitcnt vmcnt(6)
	ds_write_b128 v201, v[150:153] offset:9216
	s_waitcnt vmcnt(5)
	ds_write_b128 v200, v[154:157] offset:10240
	s_waitcnt vmcnt(4)
	ds_write_b128 v201, v[158:161] offset:11264
	s_waitcnt vmcnt(3)
	ds_write_b128 v200, v[162:165] offset:12288
	s_waitcnt vmcnt(2)
	ds_write_b128 v201, v[166:169] offset:13312
	s_waitcnt vmcnt(1)
	ds_write_b128 v200, v[170:173] offset:14336
	s_waitcnt vmcnt(0)
	ds_write_b128 v201, v[174:177] offset:15360

; #define FA_SBAR() __builtin_amdgcn_sched_barrier(0)
; #define AA_LOADKC(tile_) do { _Pragma("unroll") for (int i_ = 0; i_ < 16; ++i_) { int tk = cls + ((base + (tile_) * 64 + 4 * i_ + vkey) << sh); tk = tk < 0 ? 0 : (tk > SEQ - 1 ? SEQ - 1 : tk); \
;                     kc[i_] = *(const v4u*)(Zbc + (unsigned)tk * (NA * 2) + (ZA_K + vch * 8) * 2); } } while (0)
; #define AA_WRITEV(vv_, i0_) do { _Pragma("unroll") for (int i_ = 0; i_ < 8; ++i_) { const int i = (i0_) + i_; *(LAS v4u*)(Vl + vstb + ((i & 1) + 2 * (i >> 2)) * 2048 + ((i >> 1) & 1) * 256) = vv_[i_]; } } while (0)
; __device__ __forceinline__ void partialSM(f32x16& p0, f32x16& p1, float& m_reg, float& mn, float& alpha, const float C, const float thr) {
;     ...
;   for (int r = 0; r < 16; ++r) p0[r] = fmaf(p0[r], C, mnC);
; #pragma unroll
;   for (int r = 0; r < 16; ++r) p1[r] = fmaf(p1[r], C, mnC);
; #pragma unroll
;   for (int r = 0; r < 16; ++r) p0[r] = __builtin_amdgcn_exp2f(p0[r]);
; }
; __device__ __forceinline__ void finishSM(f32x16& p0, f32x16& p1, float alpha, float& l_reg, bf16x8& pa0, bf16x8& pa1, bf16x8& pa2, bf16x8& pa3) {
; #pragma unroll
;   for (int r = 0; r < 16; ++r) p1[r] = __builtin_amdgcn_exp2f(p1[r]);
;   float ps = 0;
; #pragma unroll
;   for (int r = 0; r < 16; ++r) ps += p0[r];
; #pragma unroll
;   for (int r = 0; r < 16; ++r) ps += p1[r];
;   { auto rr = __builtin_amdgcn_permlane32_swap(__float_as_uint(ps), __float_as_uint(ps), false, false);
;     ps = __uint_as_float(rr[0]) + __uint_as_float(rr[1]); }
;   l_reg = l_reg * alpha + ps;
;   FA_PK4(p0, 0, pa0); FA_PK4(p0, 8, pa1); FA_PK4(p1, 0, pa2); FA_PK4(p1, 8, pa3);
; template <int PASS>
; __device__ __forceinline__ void attn_a_pass(LAS unsigned char* lds_all, const bf16* ZA, bf16* Oabc, float* ML, const float* rel_bias, int gw, int ngw, int xcd, int inx, int tid) {
;     ...
;                 AA_WRITEV(vbq, 8);
;                 asm volatile("s_waitcnt lgkmcnt(0)" ::: "memory"); FA_SBAR();
;                 { const int tn = (tile + 1 < ntile) ? tile + 1 : tile; AA_LOADKC(tn); }
.LBB0_1028:
	v_cndmask_b32_e64 v190, v0, v190, s[6:7]
	v_mul_f32_e32 v0, 0xbe0293ee, v190
	v_fmamk_f32 v80, v162, 0x3e0293ee, v0
	v_fmamk_f32 v81, v163, 0x3e0293ee, v0
	v_fmamk_f32 v84, v84, 0x3e0293ee, v0
	v_fmamk_f32 v85, v85, 0x3e0293ee, v0
	v_fmamk_f32 v86, v86, 0x3e0293ee, v0
	v_fmamk_f32 v87, v87, 0x3e0293ee, v0
	v_fmamk_f32 v88, v88, 0x3e0293ee, v0
	v_fmamk_f32 v89, v89, 0x3e0293ee, v0
	v_fmamk_f32 v90, v90, 0x3e0293ee, v0
	v_fmamk_f32 v91, v91, 0x3e0293ee, v0
	v_fmamk_f32 v92, v92, 0x3e0293ee, v0
	v_fmamk_f32 v93, v93, 0x3e0293ee, v0
	v_fmamk_f32 v94, v94, 0x3e0293ee, v0
	v_fmamk_f32 v95, v95, 0x3e0293ee, v0
	v_fmamk_f32 v82, v82, 0x3e0293ee, v0
	v_fmamk_f32 v83, v83, 0x3e0293ee, v0
	v_fmamk_f32 v96, v96, 0x3e0293ee, v0
	v_fmamk_f32 v97, v97, 0x3e0293ee, v0
	v_fmamk_f32 v68, v68, 0x3e0293ee, v0
	v_fmamk_f32 v69, v69, 0x3e0293ee, v0
	v_fmamk_f32 v70, v70, 0x3e0293ee, v0
	v_fmamk_f32 v71, v71, 0x3e0293ee, v0
	v_fmamk_f32 v72, v72, 0x3e0293ee, v0
	v_fmamk_f32 v73, v73, 0x3e0293ee, v0
	v_fmamk_f32 v74, v74, 0x3e0293ee, v0
	v_fmamk_f32 v75, v75, 0x3e0293ee, v0
	v_fmamk_f32 v76, v76, 0x3e0293ee, v0
	v_fmamk_f32 v77, v77, 0x3e0293ee, v0
	v_fmamk_f32 v78, v78, 0x3e0293ee, v0
	v_fmamk_f32 v79, v79, 0x3e0293ee, v0
	v_fmamk_f32 v66, v66, 0x3e0293ee, v0
	v_fmac_f32_e32 v0, 0x3e0293ee, v67
	v_exp_f32_e32 v67, v80
	v_exp_f32_e32 v80, v81
	v_exp_f32_e32 v81, v84
	v_exp_f32_e32 v84, v85
	v_exp_f32_e32 v85, v86
	v_exp_f32_e32 v173, v66
	v_add_f32_e32 v66, 0, v67
	v_exp_f32_e32 v86, v87
	v_add_f32_e32 v66, v80, v66
	v_exp_f32_e32 v87, v88
	v_add_f32_e32 v66, v81, v66
	v_exp_f32_e32 v88, v89
	v_add_f32_e32 v66, v84, v66
	v_exp_f32_e32 v89, v90
	v_add_f32_e32 v66, v85, v66
	v_exp_f32_e32 v90, v91
	v_add_f32_e32 v66, v86, v66
	v_exp_f32_e32 v91, v92
	v_add_f32_e32 v66, v87, v66
	v_exp_f32_e32 v92, v93
	v_add_f32_e32 v66, v88, v66
	v_exp_f32_e32 v93, v94
	v_add_f32_e32 v66, v89, v66
	v_exp_f32_e32 v94, v95
	v_add_f32_e32 v66, v90, v66
	v_exp_f32_e32 v82, v82
	v_add_f32_e32 v66, v91, v66
	v_exp_f32_e32 v83, v83
	v_add_f32_e32 v66, v92, v66
	v_exp_f32_e32 v95, v96
	v_add_f32_e32 v66, v93, v66
	v_exp_f32_e32 v96, v97
	v_add_f32_e32 v66, v94, v66
	v_exp_f32_e32 v97, v68
	v_add_f32_e32 v66, v82, v66
	v_exp_f32_e32 v162, v69
	v_add_f32_e32 v66, v83, v66
	v_exp_f32_e32 v163, v70
	v_add_f32_e32 v66, v95, v66
	v_exp_f32_e32 v164, v71
	v_add_f32_e32 v66, v96, v66
	v_exp_f32_e32 v165, v72
	v_add_f32_e32 v66, v97, v66
	v_exp_f32_e32 v166, v73
	v_add_f32_e32 v66, v162, v66
	v_exp_f32_e32 v167, v74
	v_add_f32_e32 v66, v163, v66
	v_exp_f32_e32 v168, v75
	v_add_f32_e32 v66, v164, v66
	v_exp_f32_e32 v169, v76
	v_add_f32_e32 v66, v165, v66
	v_exp_f32_e32 v170, v77
	v_add_f32_e32 v66, v166, v66
	v_exp_f32_e32 v171, v78
	v_add_f32_e32 v66, v167, v66
	v_exp_f32_e32 v172, v79
	v_add_f32_e32 v66, v168, v66
	v_add_f32_e32 v66, v169, v66
	v_exp_f32_e32 v0, v0
	v_add_f32_e32 v66, v170, v66
	v_add_f32_e32 v66, v171, v66
	v_add_f32_e32 v66, v172, v66
	v_add_f32_e32 v66, v173, v66
	v_add_f32_e32 v191, v0, v66
	v_mov_b32_e32 v217, v191
	s_nop 1
	v_permlane32_swap_b32_e32 v191, v217
	v_cvt_pk_bf16_f32 v66, v67, v80
	v_cvt_pk_bf16_f32 v67, v81, v84
	v_cvt_pk_bf16_f32 v68, v85, v86
	v_cvt_pk_bf16_f32 v69, v87, v88
	v_cvt_pk_bf16_f32 v70, v89, v90
	v_cvt_pk_bf16_f32 v71, v91, v92
	v_cvt_pk_bf16_f32 v72, v93, v94
	v_cvt_pk_bf16_f32 v73, v82, v83
	v_cvt_pk_bf16_f32 v74, v95, v96
	v_cvt_pk_bf16_f32 v75, v97, v162
	v_cvt_pk_bf16_f32 v76, v163, v164
	v_cvt_pk_bf16_f32 v77, v165, v166
	v_cvt_pk_bf16_f32 v78, v167, v168
	v_cvt_pk_bf16_f32 v79, v169, v170
	v_cvt_pk_bf16_f32 v80, v171, v172
	v_cvt_pk_bf16_f32 v81, v173, v0
	s_nop 0
	v_permlane32_swap_b32_e32 v66, v68
	v_permlane32_swap_b32_e32 v67, v69
	v_permlane32_swap_b32_e32 v70, v72
	v_permlane32_swap_b32_e32 v71, v73
	v_permlane32_swap_b32_e32 v74, v76
	v_permlane32_swap_b32_e32 v75, v77
	v_permlane32_swap_b32_e32 v78, v80
	v_permlane32_swap_b32_e32 v79, v81
	s_waitcnt vmcnt(7)
	ds_write_b128 v209, v[130:133] offset:8192
	s_waitcnt vmcnt(6)
	ds_write_b128 v209, v[134:137] offset:10240
	s_waitcnt vmcnt(5)
	ds_write_b128 v209, v[138:141] offset:8448
	s_waitcnt vmcnt(4)
	ds_write_b128 v209, v[142:145] offset:10496
	s_waitcnt vmcnt(3)
	ds_write_b128 v209, v[146:149] offset:12288
	s_waitcnt vmcnt(2)
	ds_write_b128 v209, v[150:153] offset:14336
	s_waitcnt vmcnt(1)
	ds_write_b128 v209, v[154:157] offset:12544
	s_waitcnt vmcnt(0)
	ds_write_b128 v209, v[158:161] offset:14592
	s_waitcnt lgkmcnt(0)
	s_add_i32 s6, s84, 1
	s_cmp_lt_u32 s6, s89
	s_cselect_b32 s7, s6, s84
	s_cbranch_scc0 .Ldil2_noreload
; #define AA_LOADKC(tile_) do { _Pragma("unroll") for (int i_ = 0; i_ < 16; ++i_) { int tk = cls + ((base + (tile_) * 64 + 4 * i_ + vkey) << sh); tk = tk < 0 ? 0 : (tk > SEQ - 1 ? SEQ - 1 : tk); \
;                     kc[i_] = *(const v4u*)(Zbc + (unsigned)tk * (NA * 2) + (ZA_K + vch * 8) * 2); } } while (0)
; template <int PASS>
; __device__ __forceinline__ void attn_a_pass(LAS unsigned char* lds_all, const bf16* ZA, bf16* Oabc, float* ML, const float* rel_bias, int gw, int ngw, int xcd, int inx, int tid) {
;     ...
;                 { const int tn = (tile + 1 < ntile) ? tile + 1 : tile; AA_LOADKC(tn); }
	v_lshl_add_u32 v172, s7, 6, v210
	v_lshlrev_b32_e32 v0, s83, v172
	v_add_u32_e32 v0, s86, v0
	v_med3_i32 v0, v0, 0, v230
	v_mul_u32_u24_e32 v0, 0x1800, v0
	v_lshl_add_u64 v[82:83], v[192:193], 0, v[0:1]
	v_add_lshl_u32 v0, v172, 4, s83
	v_add_u32_e32 v0, s86, v0
	v_med3_i32 v0, v0, 0, v230
	v_mul_u32_u24_e32 v0, 0x1800, v0
	v_lshl_add_u64 v[86:87], v[192:193], 0, v[0:1]
	v_add_lshl_u32 v0, v172, 8, s83
	v_add_u32_e32 v0, s86, v0
	v_med3_i32 v0, v0, 0, v230
	v_mul_u32_u24_e32 v0, 0x1800, v0
	v_lshl_add_u64 v[90:91], v[192:193], 0, v[0:1]
	v_add_lshl_u32 v0, v172, 12, s83
	v_add_u32_e32 v0, s86, v0
	v_med3_i32 v0, v0, 0, v230
	v_mul_u32_u24_e32 v0, 0x1800, v0
	v_lshl_add_u64 v[94:95], v[192:193], 0, v[0:1]
	v_add_lshl_u32 v0, v172, 16, s83
	v_add_u32_e32 v0, s86, v0
	v_med3_i32 v0, v0, 0, v230
	v_mul_u32_u24_e32 v0, 0x1800, v0
	v_lshl_add_u64 v[130:131], v[192:193], 0, v[0:1]
	v_add_lshl_u32 v0, v172, 20, s83
	v_add_u32_e32 v0, s86, v0
	v_med3_i32 v0, v0, 0, v230
	v_mul_u32_u24_e32 v0, 0x1800, v0
	v_lshl_add_u64 v[134:135], v[192:193], 0, v[0:1]
	v_add_lshl_u32 v0, v172, 24, s83
	v_add_u32_e32 v0, s86, v0
	v_med3_i32 v0, v0, 0, v230
	v_mul_u32_u24_e32 v0, 0x1800, v0
	v_lshl_add_u64 v[138:139], v[192:193], 0, v[0:1]
	v_add_lshl_u32 v0, v172, 28, s83
	v_add_u32_e32 v0, s86, v0
	v_med3_i32 v0, v0, 0, v230
	v_mul_u32_u24_e32 v0, 0x1800, v0
	v_lshl_add_u64 v[142:143], v[192:193], 0, v[0:1]
	v_add_lshl_u32 v0, v172, 32, s83
	v_add_u32_e32 v0, s86, v0
	v_med3_i32 v0, v0, 0, v230
	v_mul_u32_u24_e32 v0, 0x1800, v0
	v_lshl_add_u64 v[146:147], v[192:193], 0, v[0:1]
	v_add_lshl_u32 v0, v172, 36, s83
	v_add_u32_e32 v0, s86, v0
	v_med3_i32 v0, v0, 0, v230
	v_mul_u32_u24_e32 v0, 0x1800, v0
	v_lshl_add_u64 v[150:151], v[192:193], 0, v[0:1]
	v_add_lshl_u32 v0, v172, 40, s83
	v_add_u32_e32 v0, s86, v0
	v_med3_i32 v0, v0, 0, v230
	v_mul_u32_u24_e32 v0, 0x1800, v0
	v_lshl_add_u64 v[154:155], v[192:193], 0, v[0:1]
	v_add_lshl_u32 v0, v172, 44, s83
	v_add_u32_e32 v0, s86, v0
	v_med3_i32 v0, v0, 0, v230
	v_mul_u32_u24_e32 v0, 0x1800, v0
	v_lshl_add_u64 v[158:159], v[192:193], 0, v[0:1]
	v_add_lshl_u32 v0, v172, 48, s83
	v_add_u32_e32 v0, s86, v0
	v_med3_i32 v0, v0, 0, v230
	v_mul_u32_u24_e32 v0, 0x1800, v0
	v_lshl_add_u64 v[162:163], v[192:193], 0, v[0:1]
	v_add_lshl_u32 v0, v172, 52, s83
	v_add_u32_e32 v0, s86, v0
	v_med3_i32 v0, v0, 0, v230
	v_mul_u32_u24_e32 v0, 0x1800, v0
	v_lshl_add_u64 v[166:167], v[192:193], 0, v[0:1]
	v_add_lshl_u32 v0, v172, 56, s83
	v_add_u32_e32 v0, s86, v0
	v_med3_i32 v0, v0, 0, v230
	v_mul_u32_u24_e32 v0, 0x1800, v0
	v_lshl_add_u64 v[170:171], v[192:193], 0, v[0:1]
	v_add_lshl_u32 v0, v172, 60, s83
	v_add_u32_e32 v0, s86, v0
	v_med3_i32 v0, v0, 0, v230
	v_mul_u32_u24_e32 v0, 0x1800, v0
	v_lshl_add_u64 v[174:175], v[192:193], 0, v[0:1]
	global_load_dwordx4 v[82:85], v[82:83], off offset:2048
	s_nop 0
	global_load_dwordx4 v[86:89], v[86:87], off offset:2048
	s_nop 0
	global_load_dwordx4 v[90:93], v[90:91], off offset:2048
	s_nop 0
	global_load_dwordx4 v[94:97], v[94:95], off offset:2048
	s_nop 0
	global_load_dwordx4 v[130:133], v[130:131], off offset:2048
	s_nop 0
	global_load_dwordx4 v[134:137], v[134:135], off offset:2048
	s_nop 0
	global_load_dwordx4 v[138:141], v[138:139], off offset:2048
	s_nop 0
	global_load_dwordx4 v[142:145], v[142:143], off offset:2048
	s_nop 0
	global_load_dwordx4 v[146:149], v[146:147], off offset:2048
	s_nop 0
	global_load_dwordx4 v[150:153], v[150:151], off offset:2048
	s_nop 0
	global_load_dwordx4 v[154:157], v[154:155], off offset:2048
	s_nop 0
	global_load_dwordx4 v[158:161], v[158:159], off offset:2048
	s_nop 0
	global_load_dwordx4 v[162:165], v[162:163], off offset:2048
	s_nop 0
	global_load_dwordx4 v[166:169], v[166:167], off offset:2048
	s_nop 0
	global_load_dwordx4 v[170:173], v[170:171], off offset:2048
	s_nop 0
	global_load_dwordx4 v[174:177], v[174:175], off offset:2048
; #define FA_SBAR() __builtin_amdgcn_sched_barrier(0)
; #define AA_WRITEKC() do { _Pragma("unroll") for (int i_ = 0; i_ < 16; ++i_) *(LAS v4u*)(Vl + i_ * 1024 + ((i_ & 1) ? (kst0 ^ 64) : kst0)) = kc[i_]; } while (0)
;   s16x4 l0 = tr_read<BASE + v_rd_off(D0, 0, 0)>(vb), h0 = tr_read<BASE + v_rd_off(D0, 0, 1)>(vb), l1 = tr_read<BASE + v_rd_off(D0, 1, 0)>(vb), h1 = tr_read<BASE + v_rd_off(D0, 1, 1)>(vb);
;   s16x4 l2 = tr_read<BASE + v_rd_off(D0, 2, 0)>(vb), h2 = tr_read<BASE + v_rd_off(D0, 2, 1)>(vb), l3 = tr_read<BASE + v_rd_off(D0, 3, 0)>(vb), h3 = tr_read<BASE + v_rd_off(D0, 3, 1)>(vb);
;   asm volatile("s_waitcnt lgkmcnt(0)" : "+v"(l0), "+v"(h0), "+v"(l1), "+v"(h1), "+v"(l2), "+v"(h2), "+v"(l3), "+v"(h3) :: "memory"); FA_SBAR();
;     ...
;   od = __builtin_amdgcn_mfma_f32_32x32x16_bf16(pa0, FA_PK(l0, h0), od, 0, 0, 0);
;   od = __builtin_amdgcn_mfma_f32_32x32x16_bf16(pa1, FA_PK(l1, h1), od, 0, 0, 0);
;   od = __builtin_amdgcn_mfma_f32_32x32x16_bf16(pa2, FA_PK(l2, h2), od, 0, 0, 0);
;   od = __builtin_amdgcn_mfma_f32_32x32x16_bf16(pa3, FA_PK(l3, h3), od, 0, 0, 0);
;     ...
; }
;   pv_one<0, BASE>(o[0], vb, pa0, pa1, pa2, pa3); pv_one<1, BASE>(o[1], vb, pa0, pa1, pa2, pa3); pv_one<2, BASE>(o[2], vb, pa0, pa1, pa2, pa3); pv_one<3, BASE>(o[3], vb, pa0, pa1, pa2, pa3);
; template <int PASS>
; __device__ __forceinline__ void attn_a_pass(LAS unsigned char* lds_all, const bf16* ZA, bf16* Oabc, float* ML, const float* rel_bias, int gw, int ngw, int xcd, int inx, int tid) {
;     ...
;                 pv_d0(o, vb, pa0, pa1, pa2, pa3);
;                 FA_SBAR();
;                 if (tile + 1 < ntile) AA_WRITEKC();
.Ldil2_noreload:
	s_cmp_ge_u32 s6, s89
	ds_read_b64_tr_b16 v[236:237], v199 offset:0
	ds_read_b64_tr_b16 v[238:239], v199 offset:0x800
	ds_read_b64_tr_b16 v[240:241], v199 offset:0x1000
	ds_read_b64_tr_b16 v[242:243], v199 offset:0x1800
	ds_read_b64_tr_b16 v[244:245], v199 offset:0x2000
	ds_read_b64_tr_b16 v[246:247], v199 offset:0x2800
	ds_read_b64_tr_b16 v[248:249], v199 offset:0x3000
	ds_read_b64_tr_b16 v[250:251], v199 offset:0x3800
	s_nop 0
	s_waitcnt lgkmcnt(6)
	s_nop 0
	v_mfma_f32_32x32x16_bf16 v[50:65], v[66:69], v[236:239], v[50:65]
	ds_read_b64_tr_b16 v[236:237], v199 offset:0x200
	ds_read_b64_tr_b16 v[238:239], v199 offset:0xa00
	s_waitcnt lgkmcnt(6)
	v_mfma_f32_32x32x16_bf16 v[50:65], v[70:73], v[240:243], v[50:65]
	ds_read_b64_tr_b16 v[240:241], v199 offset:0x1200
	ds_read_b64_tr_b16 v[242:243], v199 offset:0x1a00
	s_waitcnt lgkmcnt(6)
	v_mfma_f32_32x32x16_bf16 v[50:65], v[74:77], v[244:247], v[50:65]
	ds_read_b64_tr_b16 v[244:245], v199 offset:0x2200
	ds_read_b64_tr_b16 v[246:247], v199 offset:0x2a00
	s_waitcnt lgkmcnt(6)
	v_mfma_f32_32x32x16_bf16 v[50:65], v[78:81], v[248:251], v[50:65]
	ds_read_b64_tr_b16 v[248:249], v199 offset:0x3200
	ds_read_b64_tr_b16 v[250:251], v199 offset:0x3a00
	s_nop 0
	s_waitcnt lgkmcnt(6)
	s_nop 0
	v_mfma_f32_32x32x16_bf16 v[34:49], v[66:69], v[236:239], v[34:49]
	ds_read_b64_tr_b16 v[236:237], v199 offset:0x400
	ds_read_b64_tr_b16 v[238:239], v199 offset:0xc00
	s_waitcnt lgkmcnt(6)
	v_mfma_f32_32x32x16_bf16 v[34:49], v[70:73], v[240:243], v[34:49]
	ds_read_b64_tr_b16 v[240:241], v199 offset:0x1400
	ds_read_b64_tr_b16 v[242:243], v199 offset:0x1c00
	s_waitcnt lgkmcnt(6)
	v_mfma_f32_32x32x16_bf16 v[34:49], v[74:77], v[244:247], v[34:49]
	ds_read_b64_tr_b16 v[244:245], v199 offset:0x2400
	ds_read_b64_tr_b16 v[246:247], v199 offset:0x2c00
	s_waitcnt lgkmcnt(6)
	v_mfma_f32_32x32x16_bf16 v[34:49], v[78:81], v[248:251], v[34:49]
	ds_read_b64_tr_b16 v[248:249], v199 offset:0x3400
	ds_read_b64_tr_b16 v[250:251], v199 offset:0x3c00
	s_nop 0
	s_waitcnt lgkmcnt(6)
	s_nop 0
	v_mfma_f32_32x32x16_bf16 v[18:33], v[66:69], v[236:239], v[18:33]
	ds_read_b64_tr_b16 v[236:237], v199 offset:0x600
	ds_read_b64_tr_b16 v[238:239], v199 offset:0xe00
	s_waitcnt lgkmcnt(6)
	v_mfma_f32_32x32x16_bf16 v[18:33], v[70:73], v[240:243], v[18:33]
	ds_read_b64_tr_b16 v[240:241], v199 offset:0x1600
	ds_read_b64_tr_b16 v[242:243], v199 offset:0x1e00
	s_waitcnt lgkmcnt(6)
	v_mfma_f32_32x32x16_bf16 v[18:33], v[74:77], v[244:247], v[18:33]
	ds_read_b64_tr_b16 v[244:245], v199 offset:0x2600
	ds_read_b64_tr_b16 v[246:247], v199 offset:0x2e00
	s_waitcnt lgkmcnt(6)
	v_mfma_f32_32x32x16_bf16 v[18:33], v[78:81], v[248:251], v[18:33]
	ds_read_b64_tr_b16 v[248:249], v199 offset:0x3600
	ds_read_b64_tr_b16 v[250:251], v199 offset:0x3e00
	s_nop 0
	s_waitcnt lgkmcnt(6)
	s_nop 0
	v_mfma_f32_32x32x16_bf16 v[2:17], v[66:69], v[236:239], v[2:17]
	s_waitcnt lgkmcnt(4)
	v_mfma_f32_32x32x16_bf16 v[2:17], v[70:73], v[240:243], v[2:17]
	s_waitcnt lgkmcnt(2)
	v_mfma_f32_32x32x16_bf16 v[2:17], v[74:77], v[244:247], v[2:17]
	s_waitcnt lgkmcnt(0)
	v_mfma_f32_32x32x16_bf16 v[2:17], v[78:81], v[248:251], v[2:17]
	s_cbranch_scc1 .LBB0_1030
	s_waitcnt vmcnt(15)
	ds_write_b128 v211, v[82:85]
	s_waitcnt vmcnt(14)
	ds_write_b128 v208, v[86:89] offset:1024
	s_waitcnt vmcnt(13)
	ds_write_b128 v211, v[90:93] offset:2048
	s_waitcnt vmcnt(12)
	ds_write_b128 v208, v[94:97] offset:3072
	s_waitcnt vmcnt(11)
	ds_write_b128 v211, v[130:133] offset:4096
	s_waitcnt vmcnt(10)
	ds_write_b128 v208, v[134:137] offset:5120
	s_waitcnt vmcnt(9)
	ds_write_b128 v211, v[138:141] offset:6144
	s_waitcnt vmcnt(8)
	ds_write_b128 v208, v[142:145] offset:7168
	s_waitcnt vmcnt(7)
	ds_write_b128 v211, v[146:149] offset:8192
	s_waitcnt vmcnt(6)
	ds_write_b128 v208, v[150:153] offset:9216
	s_waitcnt vmcnt(5)
	ds_write_b128 v211, v[154:157] offset:10240
	s_waitcnt vmcnt(4)
	ds_write_b128 v208, v[158:161] offset:11264
	s_waitcnt vmcnt(3)
	ds_write_b128 v211, v[162:165] offset:12288
	s_waitcnt vmcnt(2)
	ds_write_b128 v208, v[166:169] offset:13312
	s_waitcnt vmcnt(1)
	ds_write_b128 v211, v[170:173] offset:14336
	s_waitcnt vmcnt(0)
	ds_write_b128 v208, v[174:177] offset:15360
